# P10 combine: the 16 serialized gate-vector loads (each with vmcnt(0)) hoisted into free quads, counted waits
# baseline (speedup 1.0000x reference)
.LBB0_2510:
	s_cmp_lg_u32 s0, s38
	s_cselect_b64 s[36:37], -1, 0
	s_min_i32 s1, s38, 0x4000
	s_lshr_b32 s1, s1, 12
	s_mul_i32 s2, s1, 0x3000
	s_ashr_i32 s3, s2, 31
	s_lshl_b64 s[44:45], s[2:3], 2
	s_add_u32 s2, s8, s44
	s_addc_u32 s3, s9, s45
	v_lshlrev_b32_e32 v146, 16, v100
	v_and_b32_e32 v147, 0xffff0000, v100
	v_lshlrev_b32_e32 v148, 16, v101
	v_and_b32_e32 v149, 0xffff0000, v101
	v_lshlrev_b32_e32 v138, 16, v96
	v_and_b32_e32 v139, 0xffff0000, v96
	v_lshlrev_b32_e32 v140, 16, v97
	v_and_b32_e32 v141, 0xffff0000, v97
	v_lshlrev_b32_e32 v130, 16, v94
	v_and_b32_e32 v131, 0xffff0000, v94
	v_lshlrev_b32_e32 v132, 16, v95
	v_and_b32_e32 v133, 0xffff0000, v95
	v_lshlrev_b32_e32 v100, 16, v90
	v_and_b32_e32 v101, 0xffff0000, v90
	v_lshlrev_b32_e32 v116, 16, v91
	v_and_b32_e32 v117, 0xffff0000, v91
	v_lshlrev_b32_e32 v94, 16, v88
	v_and_b32_e32 v95, 0xffff0000, v88
	v_lshlrev_b32_e32 v96, 16, v89
	v_and_b32_e32 v97, 0xffff0000, v89
	v_lshlrev_b32_e32 v88, 16, v84
	v_and_b32_e32 v89, 0xffff0000, v84
	v_lshlrev_b32_e32 v90, 16, v85
	v_and_b32_e32 v91, 0xffff0000, v85
	v_lshl_add_u64 v[84:85], s[2:3], 0, v[2:3]
	s_mov_b64 s[2:3], 0xa000
	v_lshl_add_u64 v[154:155], v[84:85], 0, s[2:3]
	v_add_co_u32_e32 v84, vcc, s63, v84
	s_min_i32 s0, s0, 0x4000
	s_nop 0
	v_addc_co_u32_e32 v85, vcc, 0, v85, vcc
	global_load_dwordx4 v[168:171], v[84:85], off offset:-4096
	global_load_dwordx4 v[176:179], v[154:155], off offset:1024
	global_load_dwordx4 v[184:187], v[154:155], off offset:2048
	global_load_dwordx4 v[212:215], v[154:155], off offset:3072
	global_load_dwordx4 v[224:227], v[84:85], off
	global_load_dwordx4 v[232:235], v[84:85], off offset:1024
	global_load_dwordx4 v[240:243], v[84:85], off offset:2048
	global_load_dwordx4 v[248:251], v[84:85], off offset:3072
	s_lshr_b32 s0, s0, 12
	s_mulk_i32 s0, 0x3000
	s_ashr_i32 s1, s0, 31
	s_lshl_b64 s[46:47], s[0:1], 2
	s_add_u32 s0, s8, s46
	s_addc_u32 s1, s9, s47
	v_lshlrev_b32_e32 v142, 16, v114
	v_and_b32_e32 v143, 0xffff0000, v114
	v_lshl_add_u64 v[164:165], s[0:1], 0, v[2:3]
	v_lshlrev_b32_e32 v144, 16, v115
	v_and_b32_e32 v145, 0xffff0000, v115
	v_lshlrev_b32_e32 v134, 16, v112
	v_and_b32_e32 v135, 0xffff0000, v112
	v_lshlrev_b32_e32 v136, 16, v113
	v_and_b32_e32 v137, 0xffff0000, v113
	v_lshl_add_u64 v[166:167], v[164:165], 0, s[2:3]
	global_load_dwordx4 v[180:183], v[166:167], off offset:1024
	global_load_dwordx4 v[190:193], v[166:167], off offset:2048
	global_load_dwordx4 v[216:219], v[166:167], off offset:3072
	v_lshlrev_b32_e32 v126, 16, v110
	v_and_b32_e32 v127, 0xffff0000, v110
	v_lshlrev_b32_e32 v128, 16, v111
	v_and_b32_e32 v129, 0xffff0000, v111
	v_lshlrev_b32_e32 v118, 16, v108
	v_and_b32_e32 v119, 0xffff0000, v108
	v_lshlrev_b32_e32 v120, 16, v109
	v_and_b32_e32 v121, 0xffff0000, v109
	v_lshlrev_b32_e32 v122, 16, v92
	v_and_b32_e32 v123, 0xffff0000, v92
	v_lshlrev_b32_e32 v124, 16, v93
	v_and_b32_e32 v125, 0xffff0000, v93
	v_lshlrev_b32_e32 v112, 16, v106
	v_and_b32_e32 v113, 0xffff0000, v106
	v_lshlrev_b32_e32 v114, 16, v107
	v_and_b32_e32 v115, 0xffff0000, v107
	v_lshlrev_b32_e32 v108, 16, v104
	v_and_b32_e32 v109, 0xffff0000, v104
	v_lshlrev_b32_e32 v110, 16, v105
	v_and_b32_e32 v111, 0xffff0000, v105
	v_lshlrev_b32_e32 v104, 16, v102
	v_and_b32_e32 v105, 0xffff0000, v102
	v_lshlrev_b32_e32 v106, 16, v103
	v_and_b32_e32 v107, 0xffff0000, v103
	v_lshlrev_b32_e32 v92, 16, v86
	v_and_b32_e32 v93, 0xffff0000, v86
	v_lshlrev_b32_e32 v102, 16, v98
	v_and_b32_e32 v103, 0xffff0000, v98
	v_lshlrev_b32_e32 v98, 16, v99
	v_and_b32_e32 v99, 0xffff0000, v99
	v_lshlrev_b32_e32 v86, 16, v87
	v_and_b32_e32 v87, 0xffff0000, v87
	v_readlane_b32 s2, v253, 48
	v_readlane_b32 s3, v253, 49
	s_mov_b64 s[0:1], -1
	s_waitcnt vmcnt(10)
	v_mov_b32_e32 v150, v168
	v_mov_b32_e32 v151, v169
	v_mov_b32_e32 v152, v170
	v_mov_b32_e32 v153, v171
	v_pk_fma_f32 v[64:65], v[150:151], v[64:65], v[142:143]
	v_add_co_u32_e32 v142, vcc, s63, v164
	v_pk_fma_f32 v[66:67], v[152:153], v[66:67], v[144:145]
	s_nop 0
	v_addc_co_u32_e32 v143, vcc, 0, v165, vcc
	global_load_dwordx4 v[172:175], v[142:143], off offset:-4096
	global_load_dwordx4 v[228:231], v[142:143], off
	global_load_dwordx4 v[236:239], v[142:143], off offset:1024
	global_load_dwordx4 v[244:247], v[142:143], off offset:2048
	global_load_dwordx4 v[168:171], v[142:143], off offset:3072
	s_and_b64 vcc, exec, s[2:3]
	s_waitcnt vmcnt(4)
	v_mov_b32_e32 v150, v172
	v_mov_b32_e32 v151, v173
	v_mov_b32_e32 v152, v174
	v_mov_b32_e32 v153, v175
	v_pk_fma_f32 v[60:61], v[150:151], v[60:61], v[146:147]
	v_pk_fma_f32 v[62:63], v[152:153], v[62:63], v[148:149]
	s_waitcnt vmcnt(4)
	v_mov_b32_e32 v144, v176
	v_mov_b32_e32 v145, v177
	v_mov_b32_e32 v146, v178
	v_mov_b32_e32 v147, v179
	v_pk_fma_f32 v[56:57], v[144:145], v[56:57], v[134:135]
	v_pk_fma_f32 v[58:59], v[146:147], v[58:59], v[136:137]
	s_waitcnt vmcnt(4)
	v_mov_b32_e32 v134, v180
	v_mov_b32_e32 v135, v181
	v_mov_b32_e32 v136, v182
	v_mov_b32_e32 v137, v183
	v_pk_fma_f32 v[52:53], v[134:135], v[52:53], v[138:139]
	v_pk_fma_f32 v[54:55], v[136:137], v[54:55], v[140:141]
	s_waitcnt vmcnt(4)
	v_mov_b32_e32 v134, v184
	v_mov_b32_e32 v135, v185
	v_mov_b32_e32 v136, v186
	v_mov_b32_e32 v137, v187
	v_pk_fma_f32 v[48:49], v[134:135], v[48:49], v[126:127]
	v_pk_fma_f32 v[50:51], v[136:137], v[50:51], v[128:129]
	s_waitcnt vmcnt(4)
	v_mov_b32_e32 v126, v190
	v_mov_b32_e32 v127, v191
	v_mov_b32_e32 v128, v192
	v_mov_b32_e32 v129, v193
	v_pk_fma_f32 v[44:45], v[126:127], v[44:45], v[130:131]
	v_pk_fma_f32 v[46:47], v[128:129], v[46:47], v[132:133]
	s_waitcnt vmcnt(4)
	v_mov_b32_e32 v126, v212
	v_mov_b32_e32 v127, v213
	v_mov_b32_e32 v128, v214
	v_mov_b32_e32 v129, v215
	v_pk_fma_f32 v[40:41], v[126:127], v[40:41], v[118:119]
	v_pk_fma_f32 v[42:43], v[128:129], v[42:43], v[120:121]
	v_mul_f32_e32 v140, v40, v40
	v_mul_f32_e32 v138, v42, v42
	s_waitcnt vmcnt(4)
	v_mov_b32_e32 v118, v216
	v_mov_b32_e32 v119, v217
	v_mov_b32_e32 v120, v218
	v_mov_b32_e32 v121, v219
	v_pk_fma_f32 v[36:37], v[118:119], v[36:37], v[122:123]
	v_pk_fma_f32 v[38:39], v[120:121], v[38:39], v[124:125]
	s_waitcnt vmcnt(4)
	v_mov_b32_e32 v118, v224
	v_mov_b32_e32 v119, v225
	v_mov_b32_e32 v120, v226
	v_mov_b32_e32 v121, v227
	v_pk_fma_f32 v[34:35], v[120:121], v[34:35], v[114:115]
	v_pk_fma_f32 v[32:33], v[118:119], v[32:33], v[112:113]
	v_mul_f32_e32 v128, v32, v32
	v_mul_f32_e32 v132, v33, v33
	v_mul_f32_e32 v124, v34, v34
	v_mul_f32_e32 v126, v35, v35
	s_waitcnt vmcnt(3)
	v_mov_b32_e32 v112, v228
	v_mov_b32_e32 v113, v229
	v_mov_b32_e32 v114, v230
	v_mov_b32_e32 v115, v231
	v_pk_fma_f32 v[30:31], v[114:115], v[30:31], v[116:117]
	v_pk_fma_f32 v[28:29], v[112:113], v[28:29], v[100:101]
	s_waitcnt vmcnt(3)
	v_mov_b32_e32 v112, v232
	v_mov_b32_e32 v113, v233
	v_mov_b32_e32 v114, v234
	v_mov_b32_e32 v115, v235
	v_pk_fma_f32 v[26:27], v[114:115], v[26:27], v[110:111]
	v_pk_fma_f32 v[24:25], v[112:113], v[24:25], v[108:109]
	v_pk_mul_f32 v[136:137], v[24:25], v[24:25]
	v_pk_mul_f32 v[114:115], v[44:45], v[44:45]
	v_mul_f32_e32 v112, v36, v36
	s_waitcnt vmcnt(2)
	v_mov_b32_e32 v108, v236
	v_mov_b32_e32 v109, v237
	v_mov_b32_e32 v110, v238
	v_mov_b32_e32 v111, v239
	v_pk_fma_f32 v[22:23], v[110:111], v[22:23], v[96:97]
	v_pk_fma_f32 v[20:21], v[108:109], v[20:21], v[94:95]
	v_mul_f32_e32 v110, v38, v38
	v_pk_mul_f32 v[108:109], v[20:21], v[20:21]
	s_waitcnt vmcnt(2)
	v_mov_b32_e32 v94, v240
	v_mov_b32_e32 v95, v241
	v_mov_b32_e32 v96, v242
	v_mov_b32_e32 v97, v243
	v_pk_fma_f32 v[18:19], v[96:97], v[18:19], v[106:107]
	v_pk_fma_f32 v[16:17], v[94:95], v[16:17], v[104:105]
	v_mul_f32_e32 v104, v28, v28
	v_mul_f32_e32 v106, v29, v29
	v_mul_f32_e32 v134, v16, v16
	v_mul_f32_e32 v130, v18, v18
	s_waitcnt vmcnt(1)
	v_mov_b32_e32 v94, v244
	v_mov_b32_e32 v95, v245
	v_mov_b32_e32 v96, v246
	v_mov_b32_e32 v97, v247
	v_pk_fma_f32 v[12:13], v[94:95], v[12:13], v[92:93]
	v_pk_fma_f32 v[14:15], v[96:97], v[14:15], v[86:87]
	v_mul_f32_e32 v96, v30, v30
	v_mul_f32_e32 v100, v14, v14
	s_waitcnt vmcnt(1)
	v_mov_b32_e32 v92, v248
	v_mov_b32_e32 v93, v249
	v_mov_b32_e32 v94, v250
	v_mov_b32_e32 v95, v251
	v_pk_fma_f32 v[84:85], v[94:95], v[10:11], v[98:99]
	v_pk_fma_f32 v[86:87], v[92:93], v[8:9], v[102:103]
	v_mul_f32_e32 v120, v86, v86
	v_mul_f32_e32 v122, v87, v87
	v_mul_f32_e32 v116, v84, v84
	v_mul_f32_e32 v118, v85, v85
	v_mul_f32_e32 v98, v31, v31
	v_pk_mul_f32 v[142:143], v[48:49], v[48:49]
	v_mul_f32_e32 v102, v12, v12
	s_waitcnt vmcnt(0)
	v_mov_b32_e32 v8, v168
	v_mov_b32_e32 v9, v169
	v_mov_b32_e32 v10, v170
	v_mov_b32_e32 v11, v171
	v_pk_fma_f32 v[10:11], v[10:11], v[6:7], v[90:91]
	v_pk_fma_f32 v[8:9], v[8:9], v[4:5], v[88:89]
	v_cndmask_b32_e64 v4, 0, 1, s[36:37]
	v_mul_f32_e32 v92, v8, v8
	v_mul_f32_e32 v94, v9, v9
	v_mul_f32_e32 v88, v10, v10
	v_mul_f32_e32 v90, v11, v11
	v_cmp_ne_u32_e64 s[36:37], 1, v4
	s_cbranch_vccz .LBB0_2528
	v_mov_b32_e32 v6, v65
	v_mov_b32_e32 v7, v57
	v_mov_b32_e32 v146, v67
	v_mov_b32_e32 v147, v59
	v_mov_b32_e32 v4, v64
	v_mov_b32_e32 v5, v56
	v_pk_mul_f32 v[6:7], v[6:7], v[6:7]
	v_mov_b32_e32 v144, v66
	v_mov_b32_e32 v145, v58
	v_pk_mul_f32 v[146:147], v[146:147], v[146:147]
	v_pk_fma_f32 v[4:5], v[4:5], v[4:5], v[6:7]
	v_pk_fma_f32 v[6:7], v[144:145], v[144:145], v[146:147]
	v_mov_b32_e32 v144, v142
	v_pk_add_f32 v[4:5], v[4:5], v[6:7]
	v_pk_mul_f32 v[6:7], v[50:51], v[50:51]
	v_pk_add_f32 v[4:5], v[4:5], v[4:5] op_sel_hi:[0,1]
	v_mov_b32_e32 v145, v7
	v_pk_mov_b32 v[6:7], v[142:143], v[6:7] op_sel:[1,0]
	v_pk_fma_f32 v[146:147], v[42:43], v[42:43], v[138:139] op_sel_hi:[1,1,0]
	v_pk_add_f32 v[6:7], v[6:7], v[144:145]
	v_pk_fma_f32 v[144:145], v[40:41], v[40:41], v[140:141] op_sel_hi:[1,1,0]
	v_pk_add_f32 v[6:7], v[6:7], v[6:7] op_sel_hi:[0,1]
	v_mov_b32_e32 v129, v145
	v_mov_b32_e32 v133, v147
	v_mov_b32_e32 v125, v7
	v_mov_b32_e32 v127, v5
	v_pk_add_f32 v[144:145], v[128:129], v[132:133]
	v_pk_add_f32 v[4:5], v[124:125], v[126:127]
	v_pk_mul_f32 v[6:7], v[26:27], v[26:27]
	v_pk_add_f32 v[4:5], v[144:145], v[4:5]
	v_mov_b32_e32 v144, v136
	v_mov_b32_e32 v145, v7
	v_pk_mov_b32 v[6:7], v[136:137], v[6:7] op_sel:[1,0]
	v_pk_add_f32 v[4:5], v[4:5], v[4:5] op_sel_hi:[0,1]
	v_pk_add_f32 v[6:7], v[6:7], v[144:145]
	v_pk_fma_f32 v[144:145], v[16:17], v[16:17], v[134:135] op_sel_hi:[1,1,0]
	v_pk_add_f32 v[6:7], v[6:7], v[6:7] op_sel_hi:[0,1]
	v_pk_fma_f32 v[146:147], v[18:19], v[18:19], v[130:131] op_sel_hi:[1,1,0]
	v_mov_b32_e32 v121, v145
	v_mov_b32_e32 v123, v147
	v_mov_b32_e32 v117, v7
	v_mov_b32_e32 v119, v5
	v_pk_add_f32 v[144:145], v[120:121], v[122:123]
	v_pk_add_f32 v[4:5], v[116:117], v[118:119]
	v_mov_b32_e32 v6, v61
	v_pk_add_f32 v[146:147], v[144:145], v[4:5]
	v_and_b32_e32 v5, 64, v207
	v_xor_b32_e32 v4, 16, v207
	v_add_u32_e32 v101, 64, v5
	v_cmp_lt_i32_e32 vcc, v4, v101
	v_mov_b32_e32 v7, v53
	v_mov_b32_e32 v148, v63
	v_cndmask_b32_e32 v4, v207, v4, vcc
	v_mov_b32_e32 v149, v55
	v_lshlrev_b32_e32 v103, 2, v4
	v_mov_b32_e32 v4, v60
	v_mov_b32_e32 v5, v52
	v_pk_mul_f32 v[6:7], v[6:7], v[6:7]
	v_mov_b32_e32 v144, v62
	v_mov_b32_e32 v145, v54
	v_pk_mul_f32 v[148:149], v[148:149], v[148:149]
	v_pk_fma_f32 v[4:5], v[4:5], v[4:5], v[6:7]
	v_pk_fma_f32 v[6:7], v[144:145], v[144:145], v[148:149]
	v_pk_fma_f32 v[152:153], v[36:37], v[36:37], v[112:113] op_sel_hi:[1,1,0]
	v_pk_add_f32 v[4:5], v[4:5], v[6:7]
	v_mov_b32_e32 v7, s65
	ds_read_b64 v[144:145], v7
	v_pk_add_f32 v[148:149], v[4:5], v[4:5] op_sel_hi:[0,1]
	v_pk_mul_f32 v[4:5], v[46:47], v[46:47]
	v_mov_b32_e32 v6, v114
	v_mov_b32_e32 v7, v5
	v_pk_mov_b32 v[4:5], v[114:115], v[4:5] op_sel:[1,0]
	s_waitcnt lgkmcnt(0)
	v_readfirstlane_b32 s0, v144
	v_pk_add_f32 v[4:5], v[4:5], v[6:7]
	v_readfirstlane_b32 s1, v145
	v_pk_add_f32 v[150:151], v[4:5], v[4:5] op_sel_hi:[0,1]
	v_pk_fma_f32 v[154:155], v[38:39], v[38:39], v[110:111] op_sel_hi:[1,1,0]
	v_mov_b32_e32 v105, v153
	v_mov_b32_e32 v107, v155
	v_mov_b32_e32 v97, v151
	global_load_dwordx4 v[4:7], v2, s[0:1]
	v_mov_b32_e32 v99, v149
	v_pk_add_f32 v[152:153], v[104:105], v[106:107]
	v_pk_add_f32 v[148:149], v[96:97], v[98:99]
	v_pk_mul_f32 v[150:151], v[22:23], v[22:23]
	v_pk_add_f32 v[148:149], v[152:153], v[148:149]
	v_mov_b32_e32 v152, v108
	v_mov_b32_e32 v153, v151
	v_pk_mov_b32 v[150:151], v[108:109], v[150:151] op_sel:[1,0]
	v_pk_add_f32 v[148:149], v[148:149], v[148:149] op_sel_hi:[0,1]
	v_pk_add_f32 v[150:151], v[150:151], v[152:153]
	v_pk_fma_f32 v[152:153], v[12:13], v[12:13], v[102:103] op_sel_hi:[1,1,0]
	v_pk_add_f32 v[150:151], v[150:151], v[150:151] op_sel_hi:[0,1]
	v_pk_fma_f32 v[154:155], v[14:15], v[14:15], v[100:101] op_sel_hi:[1,1,0]
	v_mov_b32_e32 v93, v153
	v_mov_b32_e32 v95, v155
	v_mov_b32_e32 v89, v151
	v_mov_b32_e32 v91, v149
	v_pk_add_f32 v[152:153], v[92:93], v[94:95]
	v_pk_add_f32 v[148:149], v[88:89], v[90:91]
	v_mov_b32_e32 v151, v146
	v_pk_add_f32 v[148:149], v[152:153], v[148:149]
	v_xor_b32_e32 v89, 32, v207
	v_mov_b32_e32 v150, v148
	v_mov_b32_e32 v146, v149
	v_pk_add_f32 v[146:147], v[150:151], v[146:147]
	v_cmp_lt_i32_e32 vcc, v89, v101
	s_mov_b32 s0, 0x3a000000
	v_mov_b32_dpp v149, v147 quad_perm:[1,0,3,2] row_mask:0xf bank_mask:0xf bound_ctrl:1
	v_mov_b32_dpp v148, v146 quad_perm:[1,0,3,2] row_mask:0xf bank_mask:0xf bound_ctrl:1
	v_pk_add_f32 v[146:147], v[146:147], v[148:149]
	v_cndmask_b32_e32 v89, v207, v89, vcc
	v_lshlrev_b32_e32 v89, 2, v89
	v_mov_b32_dpp v149, v147 quad_perm:[2,3,0,1] row_mask:0xf bank_mask:0xf bound_ctrl:1
	v_mov_b32_dpp v148, v146 quad_perm:[2,3,0,1] row_mask:0xf bank_mask:0xf bound_ctrl:1
	v_pk_add_f32 v[146:147], v[146:147], v[148:149]
	s_nop 1
	v_mov_b32_dpp v149, v147 row_half_mirror row_mask:0xf bank_mask:0xf bound_ctrl:1
	v_mov_b32_dpp v148, v146 row_half_mirror row_mask:0xf bank_mask:0xf bound_ctrl:1
	v_pk_add_f32 v[146:147], v[146:147], v[148:149]
	s_nop 1
	v_mov_b32_dpp v149, v147 row_mirror row_mask:0xf bank_mask:0xf bound_ctrl:1
	v_mov_b32_dpp v148, v146 row_mirror row_mask:0xf bank_mask:0xf bound_ctrl:1
	v_pk_add_f32 v[146:147], v[146:147], v[148:149]
	ds_bpermute_b32 v149, v103, v147
	ds_bpermute_b32 v148, v103, v146
	s_waitcnt lgkmcnt(0)
	v_pk_add_f32 v[146:147], v[146:147], v[148:149]
	ds_bpermute_b32 v149, v89, v147
	ds_bpermute_b32 v148, v89, v146
	s_waitcnt lgkmcnt(0)
	v_pk_add_f32 v[146:147], v[146:147], v[148:149]
	s_nop 0
	v_pk_fma_f32 v[146:147], v[146:147], s[0:1], v[188:189] op_sel_hi:[1,0,0]
	s_nop 0
	v_mul_f32_e32 v89, 0x4b800000, v147
	v_cmp_gt_f32_e32 vcc, s11, v147
	v_mul_f32_e32 v91, 0x4b800000, v146
	v_cmp_gt_f32_e64 s[0:1], s11, v146
	v_cndmask_b32_e32 v89, v147, v89, vcc
	v_rsq_f32_e32 v89, v89
	v_cndmask_b32_e64 v91, v146, v91, s[0:1]
	v_rsq_f32_e32 v91, v91
	v_mul_f32_e32 v93, 0x45800000, v89
	v_cndmask_b32_e32 v150, v89, v93, vcc
	v_mul_f32_e32 v89, 0x45800000, v91
	v_cndmask_b32_e64 v148, v91, v89, s[0:1]
	s_lshl_b64 s[0:1], s[42:43], 2
	s_add_u32 s0, s16, s0
	s_addc_u32 s1, s17, s1
	s_lshl_b64 s[2:3], s[40:41], 2
	s_add_u32 s2, s16, s2
	s_addc_u32 s3, s17, s3
	v_pk_mul_f32 v[152:153], v[150:151], v[64:65] op_sel_hi:[0,1]
	v_pk_mul_f32 v[154:155], v[150:151], v[66:67] op_sel_hi:[0,1]
	v_mov_b32_e32 v149, v148
	v_lshl_add_u64 v[146:147], s[2:3], 0, v[2:3]
	s_waitcnt vmcnt(0)
	v_pk_mul_f32 v[154:155], v[154:155], v[6:7]
	v_pk_mul_f32 v[152:153], v[152:153], v[4:5]
	s_and_b64 vcc, exec, s[36:37]
	global_store_dwordx4 v2, v[152:155], s[0:1]
	s_cbranch_vccnz .LBB0_2513
	s_nop 0
	v_mov_b32_e32 v152, v148
	v_mov_b32_e32 v153, v148
	v_pk_mul_f32 v[152:153], v[152:153], v[62:63]
	v_pk_mul_f32 v[154:155], v[148:149], v[60:61]
	v_pk_mul_f32 v[6:7], v[152:153], v[6:7]
	v_pk_mul_f32 v[4:5], v[154:155], v[4:5]
	global_store_dwordx4 v[146:147], v[4:7], off
